# strategy 7.4 other half: static s_setprio 1 for waves 0-3 at mixer-phase entry
# speedup vs baseline: 1.0010x; 1.0010x over previous
; #define GRID_BAR() do { XcdBarrier bb_ = bar; GAS unsigned* gb_ = (GAS unsigned*)bar.bar; asm volatile("" : "+s"(gb_), "+s"(bb_.x)); bb_.bar = (unsigned*)gb_; xcd_barrier(bb_); } while (0)
; __global__ void __launch_bounds__(NWAVES * 64, 2) mega_fwd(Args args) {
;     ...
;         if (IN(pb + 2)) for (int rep = 0; rep < REPS(3, l); ++rep) {
;             if (rep) GRID_BAR();
;             { PHASE_CTX();
;             const bf16_t* PROJ = (const bf16_t*)(ws + WS_PROJ); bf16_t* Y = (bf16_t*)(ws + WS_Y);
;             const bf16_t* mkv = (const bf16_t*)(ws + WS_MKV) + (size_t)l * MEMR * 2048;
;             gu32* qhead = (gu32*)(ws + WS_CTL) + CW_Q + 64 * (l + 2 * rep);
;             const float lam_init = l == 0 ? 0.2f : 0.35550907f;
;             for (;;) {
;                 if (tid == 0) MISC[16] = __hip_atomic_fetch_add(qhead, 1u, RLX_AGENT);
;                 __syncthreads(); const int uq = (int)MISC[16]; __syncthreads();
;                 int lane_u = lane; asm volatile("" : "+v"(lane_u));
;                 constexpr int NCONV = CONV_NCH;
;                 int u = uq; bool xtra = false; (void)xtra;
.LBB0_423:
	v_readlane_b32 s10, v253, 41
	v_readlane_b32 s0, v253, 34
	v_mov_b32_e32 v1, 0x3eb60549
	v_mov_b32_e32 v2, 0x3e4ccccd
	v_readlane_b32 s1, v253, 35
	s_mov_b32 s12, s10
	v_readlane_b32 s11, v253, 42
	v_cndmask_b32_e64 v203, v1, v2, s[0:1]
	v_writelane_b32 v253, s12, 41
	v_mov_b32_e32 v1, v0
	s_mov_b32 s11, s3
	v_writelane_b32 v253, s13, 42
	s_lshl_b64 s[6:7], s[10:11], 22
	v_readfirstlane_b32 s12, v1
	s_lshl_b32 s2, s10, 7
	s_lshl_b32 s0, s10, 8
	s_lshl_b64 s[8:9], s[10:11], 21
	s_lshl_b32 s4, s10, 10
	s_lshl_b64 s[10:11], s[10:11], 19
	v_readlane_b32 s20, v252, 6
	s_ashr_i32 s14, s12, 6
	s_cmp_lt_i32 s14, 4
	s_cbranch_scc0 .Lmix_prio_done
	s_setprio 1
